# v010 + MoE up-projection unit order: row-panel group size 2 -> 4 (more CUs of an XCD share each expert-weight tile)
# baseline (speedup 1.0000x reference)
;     __host__ __device__ bool next(int i, Unit& u) const {
;         const long L = (long)i * G + c; if (L >= nwg) return false;
;         int wgid = (int)L; { const int q = nwg / NXCD, r = nwg % NXCD, xcd = wgid % NXCD; int off = wgid / NXCD; if (rev & 2) off = (xcd < r ? q + 1 : q) - 1 - off;
;             wgid = (xcd < r ? xcd * (q + 1) : r * (q + 1) + (xcd - r) * q) + off; }
;         const int nig = wgm * nN, gid = wgid / nig, fm = gid * wgm, gsz = (nM - fm) < wgm ? (nM - fm) : wgm;
;         u.pm = fm + ((wgid % nig) % gsz); u.pn = (wgid % nig) / gsz; if (rev & 1) u.pn = nN - 1 - u.pn; return true;
.LBB13_1426:
	s_add_i32 s4, s5, s39
	s_mul_hi_i32 s5, s4, 0x92492493
	s_add_i32 s5, s5, s4
	s_lshr_b32 s12, s5, 31
	s_ashr_i32 s5, s5, 6
	s_add_i32 s5, s5, s12
	s_lshl_b32 s12, s5, 2
	s_sub_i32 s13, s3, s12
	s_min_i32 s13, s13, 4
	s_abs_i32 s18, s13
	v_cvt_f32_u32_e32 v1, s18
	s_sub_i32 s20, 0, s18
	s_mul_i32 s5, s5, 112
	s_sub_i32 s4, s4, s5
	v_rcp_iflag_f32_e32 v1, v1
	s_abs_i32 s5, s4
	s_xor_b32 s19, s4, s13
	s_ashr_i32 s19, s19, 31
	v_mul_f32_e32 v1, 0x4f7ffffe, v1
	v_cvt_u32_f32_e32 v1, v1
	s_nop 0
	v_readfirstlane_b32 s21, v1
	s_mul_i32 s20, s20, s21
	s_mul_hi_u32 s20, s21, s20
	s_add_i32 s21, s21, s20
	s_mul_hi_u32 s20, s5, s21
	s_mul_i32 s21, s20, s18
	s_sub_i32 s5, s5, s21
	s_add_i32 s22, s20, 1
	s_sub_i32 s21, s5, s18
	s_cmp_ge_u32 s5, s18
	s_cselect_b32 s20, s22, s20
	s_cselect_b32 s5, s21, s5
	s_add_i32 s21, s20, 1
	s_cmp_ge_u32 s5, s18
	s_cselect_b32 s5, s21, s20
	s_xor_b32 s5, s5, s19
	s_sub_i32 s28, s5, s19
	s_mul_i32 s5, s28, s13
	s_sub_i32 s4, s4, s5
	s_add_i32 s30, s12, s4

;     __host__ __device__ bool next(int i, Unit& u) const {
;         const long L = (long)i * G + c; if (L >= nwg) return false;
;         int wgid = (int)L; { const int q = nwg / NXCD, r = nwg % NXCD, xcd = wgid % NXCD; int off = wgid / NXCD; if (rev & 2) off = (xcd < r ? q + 1 : q) - 1 - off;
;             wgid = (xcd < r ? xcd * (q + 1) : r * (q + 1) + (xcd - r) * q) + off; }
;         const int nig = wgm * nN, gid = wgid / nig, fm = gid * wgm, gsz = (nM - fm) < wgm ? (nM - fm) : wgm;
;         u.pm = fm + ((wgid % nig) % gsz); u.pn = (wgid % nig) / gsz; if (rev & 1) u.pn = nN - 1 - u.pn; return true;
.LBB13_1438:
	s_ashr_i32 s2, s2, 3
	s_add_i32 s2, s25, s2
	s_mul_hi_i32 s6, s2, 0x92492493
	s_add_i32 s6, s6, s2
	s_lshr_b32 s7, s6, 31
	s_ashr_i32 s6, s6, 6
	s_add_i32 s6, s6, s7
	s_lshl_b32 s7, s6, 2
	s_sub_i32 s24, s3, s7
	s_min_i32 s25, s24, 4
	s_abs_i32 s24, s25
	v_cvt_f32_u32_e32 v2, s24
	s_sub_i32 s27, 0, s24
	s_mul_i32 s6, s6, 112
	s_sub_i32 s2, s2, s6
	v_rcp_iflag_f32_e32 v2, v2
	s_abs_i32 s6, s2
	s_xor_b32 s26, s2, s25
	s_ashr_i32 s26, s26, 31
	v_mul_f32_e32 v2, 0x4f7ffffe, v2
	v_cvt_u32_f32_e32 v2, v2
	s_nop 0
	v_readfirstlane_b32 s29, v2
	s_mul_i32 s27, s27, s29
	s_mul_hi_u32 s27, s29, s27
	s_add_i32 s29, s29, s27
	s_mul_hi_u32 s27, s6, s29
	s_mul_i32 s29, s27, s24
	s_sub_i32 s6, s6, s29
	s_add_i32 s36, s27, 1
	s_sub_i32 s29, s6, s24
	s_cmp_ge_u32 s6, s24
	s_cselect_b32 s27, s36, s27
	s_cselect_b32 s6, s29, s6
	s_add_i32 s29, s27, 1
	s_cmp_ge_u32 s6, s24
	s_cselect_b32 s6, s29, s27
	s_xor_b32 s6, s6, s26
	s_sub_i32 s24, s6, s26
	s_mul_i32 s6, s24, s25
	s_sub_i32 s2, s2, s6
	s_add_i32 s26, s7, s2
